# odd XCDs start the merge-to-w_xo window two s_sleep late (second timing)
# baseline (speedup 1.0000x reference)
; #define OPAQUE_WS() unsigned char* ws = P.ws; asm volatile("" : "+s"(ws)); F.ws = ws; F.tid = fresh_tid(F.wave); asm volatile("" : "+v"(F.tid)); F.lane = F.tid & 63; int c = F.bid; asm volatile("" : "+s"(c))
; #define REP_BEGIN(k) for (int rep_ = 0, nrep_ = ((k) >= PROBE_LO && (k) < PROBE_HI) ? PROBE_N : 0; rep_ <= nrep_; ++rep_) { const bool rerun = PROBE_AFTER ? (rep_ > 0) : (rep_ < nrep_), dry = rerun && PROBE_DRY_;
;     __device__ __forceinline__ bool next(int i, pg8::Unit& u) const {
;         const int t = i / 3, sub = i - 3 * t; const long L = (long)t * G + c; if (L >= (long)nM * nN) return false;
;         pg8::tile_order((int)L, nM, nN, u.pm, u.pn); u.sub = sub;
;         const size_t ao = sub == 0 ? AR_QA : sub == 1 ? AR_PB : AR_QC;
;         u.a = (const char*)ws + ao + (size_t)u.pm * 256 * K * 2; u.b = (const char*)ws + WB_WBR + (size_t)(l * 3 + sub) * SZ_WBR + (size_t)u.pn * 256 * K * 2; return true;
;     }
; __global__ void __launch_bounds__(NTHREADS, 2) mk_fwd(Params P) {
;     ...
;         if (PH_EN(2) && IN(pb + 2)) { REP_BEGIN(pb + 2) OPAQUE_WS(); int lq = l; asm volatile("" : "+s"(lq));
;             SchedMerge Sg{ws, lq, NTOK / 256, D / 256, 512, G, c};
;             EpiMerge E{ws, dry};
;             pg8::gemm_phase<EpiMerge, SchedMerge>(F.lds, 512, Sg, E, F.wave);
.LBB0_947:
	s_or_b64 exec, exec, s[0:1]
	v_readlane_b32 s0, v253, 0
	s_bitcmp1_b32 s100, 0
	s_cbranch_scc0 .Lxs_done
	s_bitcmp1_b32 s0, 0
	s_cbranch_scc0 .Lxs_done
	s_movk_i32 s0, 2
.Lxs_loop:
	s_sleep 127
	s_add_i32 s0, s0, -1
	s_cmp_lg_u32 s0, 0
	s_cbranch_scc1 .Lxs_loop
.Lxs_done:
	v_readlane_b32 s0, v253, 1
	v_readlane_b32 s1, v253, 2
	s_mov_b32 s2, 0
	s_waitcnt lgkmcnt(0)
	s_barrier
	v_readlane_b32 s28, v253, 0
	v_mbcnt_lo_u32_b32 v0, -1, s2
	v_mbcnt_hi_u32_b32 v0, -1, v0
	v_add_u32_e32 v0, s94, v0
	v_readlane_b32 s2, v255, 20
	s_mov_b32 s44, s2
	s_mov_b32 s2, s93
	s_ashr_i32 s29, s28, 31
	v_mbcnt_lo_u32_b32 v0, -1, s2
	v_mbcnt_hi_u32_b32 v0, -1, v0
	v_readlane_b32 s3, v255, 21
	v_add_u32_e32 v0, s94, v0
	s_cmpk_lt_i32 s28, 0x200
	s_cselect_b64 s[2:3], -1, 0
	s_cmpk_gt_i32 s28, 0x1ff
	v_readfirstlane_b32 s10, v0
	s_cbranch_scc1 .LBB0_953
	s_ashr_i32 s4, s28, 31
	s_lshr_b32 s4, s4, 29
	s_add_i32 s6, s28, s4
	s_and_b32 s4, s6, -8
	s_sub_i32 s7, s28, s4
	s_cmp_gt_i32 s7, -1
	s_mov_b64 s[4:5], -1
	s_cbranch_scc0 .LBB0_950
	s_lshl_b32 s8, s7, 6
	s_mov_b64 s[4:5], 0
